# plus merged dual GEMM: sub-unit 0 peeled first iteration with C=0 first-touch MFMAs, per-unit accumulator clear block removed
# speedup vs baseline: 1.0109x; 1.0048x over previous
.LBB0_438:
	s_cmp_lg_u32 s80, 0
	s_cselect_b64 s[94:95], -1, 0
	s_cmp_eq_u32 s80, 0
	s_cselect_b64 vcc, -1, 0
	s_and_b64 s[4:5], vcc, exec
	s_mov_b32 s5, 0x40000
	s_cselect_b32 s50, s36, s12
	s_cselect_b32 s4, s20, s21
	s_cselect_b32 s48, s5, 0x10000
	s_cselect_b32 s5, s38, s93
	s_cselect_b32 s52, s91, s81
	s_cselect_b32 s62, 18, 16
	s_cselect_b32 s63, s39, s96
	s_cselect_b32 s64, s19, s97
	s_cselect_b32 s47, 4, 16
	s_ashr_i32 s51, s50, 31
	s_lshl_b64 s[50:51], s[50:51], 1
	s_lshl_b64 s[50:51], s[50:51], s62
	s_add_u32 s50, s52, s50
	s_addc_u32 s51, s5, s51
	s_and_b64 s[52:53], s[56:57], exec
	s_cselect_b32 s66, s51, s59
	s_cselect_b32 s67, s50, s58
	s_ashr_i32 s5, s4, 31
	s_lshl_b64 s[4:5], s[4:5], 1
	s_lshl_b64 s[4:5], s[4:5], s62
	s_add_u32 s52, s63, s4
	s_addc_u32 s53, s64, s5
	s_and_b64 s[4:5], s[56:57], exec
	s_cselect_b32 s68, s53, s1
	s_cselect_b32 s69, s52, s0
	s_add_u32 s70, s0, 0x100
	s_addc_u32 s71, s1, 0
	s_add_u32 s0, s58, s60
	s_addc_u32 s1, s59, s61
	s_add_u32 s0, s0, 0x80
	v_mov_b32_e32 v133, v49
	v_mov_b32_e32 v135, v49
	s_addc_u32 s1, s1, 0
	s_mov_b32 s49, 0
	v_lshl_add_u64 v[50:51], s[0:1], 0, v[132:133]
	v_lshl_add_u64 v[136:137], s[0:1], 0, v[134:135]
	s_lshl_b32 s0, s47, 7
	v_cndmask_b32_e32 v207, v196, v208, vcc
	v_cndmask_b32_e32 v209, v198, v210, vcc
	v_cndmask_b32_e32 v213, v200, v212, vcc
	v_cndmask_b32_e32 v211, v206, v214, vcc
	s_add_i32 s72, s0, 0xffffff00
	s_mov_b64 s[0:1], 0
	s_mov_b32 s73, s49
	s_cmp_lg_u32 s80, 0
	s_cbranch_scc1 .LBB0_439
	s_cmp_eq_u32 s72, s0
	s_cselect_b64 s[64:65], -1, 0
	s_add_i32 s73, s73, 2
	s_add_u32 s4, s58, s0
	s_addc_u32 s5, s59, s1
	s_add_u32 s62, s4, 0x100
	s_addc_u32 s63, s5, 0
	s_and_b64 s[4:5], s[64:65], exec
	s_cselect_b32 s5, s66, s63
	s_cselect_b32 s4, s67, s62
	s_and_b64 vcc, s[56:57], s[64:65]
	s_and_b64 s[62:63], vcc, exec
	s_cselect_b32 s63, 0, s61
	s_cselect_b32 s62, s48, s60
	s_add_u32 s74, s70, s0
	s_addc_u32 s75, s71, s1
	s_and_b64 s[64:65], s[64:65], exec
	s_cselect_b32 s65, s68, s75
	s_cselect_b32 s64, s69, s74
	s_add_i32 s74, 0, 0x10000
	v_add_u32_e32 v133, s74, v197
	s_add_i32 s76, 0, 0x14000
	ds_read_b128 v[140:143], v133
	ds_read_b128 v[144:147], v133 offset:1024
	ds_read_b128 v[148:151], v133 offset:2048
	ds_read_b128 v[152:155], v133 offset:3072
	v_add_u32_e32 v133, s76, v197
	ds_read_b128 v[156:159], v133
	ds_read_b128 v[160:163], v133 offset:1024
	ds_read_b128 v[164:167], v133 offset:2048
	ds_read_b128 v[168:171], v133 offset:3072
	v_cndmask_b32_e32 v226, v132, v207, vcc
	v_cndmask_b32_e32 v48, v138, v209, vcc
	v_cndmask_b32_e32 v234, v134, v213, vcc
	v_cndmask_b32_e32 v240, v139, v211, vcc
	v_lshl_add_u64 v[242:243], v[50:51], 0, s[0:1]
	s_add_i32 m0, s37, 0xc000
	ds_read_b128 v[172:175], v201
	ds_read_b128 v[176:179], v201 offset:1024
	ds_read_b128 v[180:183], v201 offset:2048
	ds_read_b128 v[184:187], v201 offset:3072
	ds_read_b128 v[188:191], v201 offset:4096
	ds_read_b128 v[192:195], v201 offset:5120
	ds_read_b128 v[202:205], v201 offset:6144
	ds_read_b128 v[222:225], v201 offset:7168
	global_load_lds_dwordx4 v[242:243], off
	v_lshl_add_u64 v[242:243], v[136:137], 0, s[0:1]
	s_add_i32 m0, s37, 0xe000
	s_nop 0
	global_load_lds_dwordx4 v[242:243], off
	s_waitcnt vmcnt(8)
	s_waitcnt lgkmcnt(0)
	s_barrier
	s_setprio 1
	s_waitcnt lgkmcnt(0)
	v_mfma_f32_16x16x32_bf16 v[128:131], v[140:143], v[172:175], 0
	v_mfma_f32_16x16x32_bf16 v[120:123], v[148:151], v[172:175], 0
	v_mfma_f32_16x16x32_bf16 v[112:115], v[140:143], v[180:183], 0
	v_mfma_f32_16x16x32_bf16 v[104:107], v[148:151], v[180:183], 0
	v_mfma_f32_16x16x32_bf16 v[96:99], v[140:143], v[188:191], 0
	v_mfma_f32_16x16x32_bf16 v[88:91], v[148:151], v[188:191], 0
	v_mfma_f32_16x16x32_bf16 v[80:83], v[140:143], v[202:205], 0
	v_mfma_f32_16x16x32_bf16 v[72:75], v[148:151], v[202:205], 0
	v_mfma_f32_16x16x32_bf16 v[128:131], v[144:147], v[176:179], v[128:131]
	v_mfma_f32_16x16x32_bf16 v[120:123], v[152:155], v[176:179], v[120:123]
	v_mfma_f32_16x16x32_bf16 v[112:115], v[144:147], v[184:187], v[112:115]
	v_mfma_f32_16x16x32_bf16 v[104:107], v[152:155], v[184:187], v[104:107]
	v_mfma_f32_16x16x32_bf16 v[96:99], v[144:147], v[192:195], v[96:99]
	v_mfma_f32_16x16x32_bf16 v[88:91], v[152:155], v[192:195], v[88:91]
	v_mfma_f32_16x16x32_bf16 v[80:83], v[144:147], v[222:225], v[80:83]
	v_mfma_f32_16x16x32_bf16 v[72:75], v[152:155], v[222:225], v[72:75]
	s_setprio 0
	s_setprio 1
	v_mfma_f32_16x16x32_bf16 v[64:67], v[156:159], v[172:175], 0
	v_mfma_f32_16x16x32_bf16 v[60:63], v[164:167], v[172:175], 0
	v_mfma_f32_16x16x32_bf16 v[56:59], v[156:159], v[180:183], 0
	v_mfma_f32_16x16x32_bf16 v[52:55], v[164:167], v[180:183], 0
	v_mfma_f32_16x16x32_bf16 v[44:47], v[156:159], v[188:191], 0
	v_mfma_f32_16x16x32_bf16 v[40:43], v[164:167], v[188:191], 0
	v_mfma_f32_16x16x32_bf16 v[36:39], v[156:159], v[202:205], 0
	v_mfma_f32_16x16x32_bf16 v[32:35], v[164:167], v[202:205], 0
	v_mfma_f32_16x16x32_bf16 v[64:67], v[160:163], v[176:179], v[64:67]
	v_mfma_f32_16x16x32_bf16 v[60:63], v[168:171], v[176:179], v[60:63]
	v_mfma_f32_16x16x32_bf16 v[56:59], v[160:163], v[184:187], v[56:59]
	v_mfma_f32_16x16x32_bf16 v[52:55], v[168:171], v[184:187], v[52:55]
	v_mfma_f32_16x16x32_bf16 v[44:47], v[160:163], v[192:195], v[44:47]
	v_mfma_f32_16x16x32_bf16 v[40:43], v[168:171], v[192:195], v[40:43]
	v_mfma_f32_16x16x32_bf16 v[36:39], v[160:163], v[222:225], v[36:39]
	v_mfma_f32_16x16x32_bf16 v[32:35], v[168:171], v[222:225], v[32:35]
	s_setprio 0
	s_barrier
	s_add_i32 s74, s74, s9
	s_mov_b32 m0, s74
	ds_read_b128 v[172:175], v201 offset:16384
	ds_read_b128 v[176:179], v201 offset:17408
	ds_read_b128 v[180:183], v201 offset:18432
	ds_read_b128 v[184:187], v201 offset:19456
	ds_read_b128 v[188:191], v201 offset:20480
	ds_read_b128 v[192:195], v201 offset:21504
	ds_read_b128 v[202:205], v201 offset:22528
	ds_read_b128 v[222:225], v201 offset:23552
	global_load_lds_dwordx4 v48, s[64:65]
	s_add_i32 m0, s74, 0x2000
	s_lshr_b64 s[74:75], s[62:63], 2
	s_add_u32 s74, s64, s74
	s_addc_u32 s75, s65, s75
	s_add_i32 s76, s76, s9
	global_load_lds_dwordx4 v240, s[64:65]
	s_mov_b32 m0, s76
	v_mov_b32_e32 v241, v49
	global_load_lds_dwordx4 v48, s[74:75]
	s_add_i32 m0, s76, 0x2000
	v_mov_b32_e32 v227, v49
	global_load_lds_dwordx4 v240, s[74:75]
	s_mov_b32 m0, s37
	v_mov_b32_e32 v235, v49
	global_load_lds_dwordx4 v226, s[4:5]
	s_mov_b32 m0, s10
	v_lshl_add_u64 v[242:243], s[64:65], 0, v[48:49]
	global_load_lds_dwordx4 v234, s[4:5]
	s_waitcnt vmcnt(8)
	s_waitcnt lgkmcnt(0)
	v_lshl_add_u64 v[244:245], s[64:65], 0, v[240:241]
	v_lshl_add_u64 v[246:247], s[74:75], 0, v[48:49]
	v_lshl_add_u64 v[240:241], s[74:75], 0, v[240:241]
	v_lshl_add_u64 v[248:249], s[4:5], 0, v[226:227]
	v_lshl_add_u64 v[250:251], s[4:5], 0, v[234:235]
	s_barrier
	s_setprio 1
	s_waitcnt lgkmcnt(0)
	v_mfma_f32_16x16x32_bf16 v[28:31], v[140:143], v[172:175], 0
	v_mfma_f32_16x16x32_bf16 v[24:27], v[148:151], v[172:175], 0
	v_mfma_f32_16x16x32_bf16 v[20:23], v[140:143], v[180:183], 0
	v_mfma_f32_16x16x32_bf16 v[16:19], v[148:151], v[180:183], 0
	v_mfma_f32_16x16x32_bf16 v[12:15], v[140:143], v[188:191], 0
	v_mfma_f32_16x16x32_bf16 v[8:11], v[148:151], v[188:191], 0
	v_mfma_f32_16x16x32_bf16 v[4:7], v[140:143], v[202:205], 0
	v_mfma_f32_16x16x32_bf16 v[0:3], v[148:151], v[202:205], 0
	v_mfma_f32_16x16x32_bf16 v[28:31], v[144:147], v[176:179], v[28:31]
	v_mfma_f32_16x16x32_bf16 v[24:27], v[152:155], v[176:179], v[24:27]
	v_mfma_f32_16x16x32_bf16 v[20:23], v[144:147], v[184:187], v[20:23]
	v_mfma_f32_16x16x32_bf16 v[16:19], v[152:155], v[184:187], v[16:19]
	v_mfma_f32_16x16x32_bf16 v[12:15], v[144:147], v[192:195], v[12:15]
	v_mfma_f32_16x16x32_bf16 v[8:11], v[152:155], v[192:195], v[8:11]
	v_mfma_f32_16x16x32_bf16 v[4:7], v[144:147], v[222:225], v[4:7]
	v_mfma_f32_16x16x32_bf16 v[0:3], v[152:155], v[222:225], v[0:3]
	s_setprio 0
	s_setprio 1
	v_mfma_f32_16x16x32_bf16 v[68:71], v[156:159], v[172:175], 0
	v_mfma_f32_16x16x32_bf16 v[76:79], v[164:167], v[172:175], 0
	v_mfma_f32_16x16x32_bf16 v[84:87], v[156:159], v[180:183], 0
	v_mfma_f32_16x16x32_bf16 v[92:95], v[164:167], v[180:183], 0
	v_mfma_f32_16x16x32_bf16 v[100:103], v[156:159], v[188:191], 0
	v_mfma_f32_16x16x32_bf16 v[108:111], v[164:167], v[188:191], 0
	v_mfma_f32_16x16x32_bf16 v[116:119], v[156:159], v[202:205], 0
	v_mfma_f32_16x16x32_bf16 v[124:127], v[164:167], v[202:205], 0
	v_mfma_f32_16x16x32_bf16 v[68:71], v[160:163], v[176:179], v[68:71]
	v_mfma_f32_16x16x32_bf16 v[76:79], v[168:171], v[176:179], v[76:79]
	v_mfma_f32_16x16x32_bf16 v[84:87], v[160:163], v[184:187], v[84:87]
	v_mfma_f32_16x16x32_bf16 v[92:95], v[168:171], v[184:187], v[92:95]
	v_mfma_f32_16x16x32_bf16 v[100:103], v[160:163], v[192:195], v[100:103]
	v_mfma_f32_16x16x32_bf16 v[108:111], v[168:171], v[192:195], v[108:111]
	v_mfma_f32_16x16x32_bf16 v[116:119], v[160:163], v[222:225], v[116:119]
	v_mfma_f32_16x16x32_bf16 v[124:127], v[168:171], v[222:225], v[124:127]
	s_setprio 0
	s_barrier
	s_add_i32 s64, 0, 0x18000
	v_add_u32_e32 v48, s64, v197
	s_add_i32 s65, 0, 0x1c000
	ds_read_b128 v[140:143], v48
	ds_read_b128 v[144:147], v48 offset:1024
	ds_read_b128 v[148:151], v48 offset:2048
	ds_read_b128 v[152:155], v48 offset:3072
	v_add_u32_e32 v48, s65, v197
	ds_read_b128 v[156:159], v48
	ds_read_b128 v[160:163], v48 offset:1024
	ds_read_b128 v[164:167], v48 offset:2048
	ds_read_b128 v[168:171], v48 offset:3072
	s_add_u32 s4, s4, s62
	s_addc_u32 s5, s5, s63
	s_mov_b32 m0, s8
	ds_read_b128 v[172:175], v201 offset:32768
	ds_read_b128 v[176:179], v201 offset:33792
	ds_read_b128 v[180:183], v201 offset:34816
	ds_read_b128 v[184:187], v201 offset:35840
	ds_read_b128 v[188:191], v201 offset:36864
	ds_read_b128 v[192:195], v201 offset:37888
	ds_read_b128 v[202:205], v201 offset:38912
	ds_read_b128 v[222:225], v201 offset:39936
	global_load_lds_dwordx4 v226, s[4:5]
	s_mov_b32 m0, s18
	s_nop 0
	global_load_lds_dwordx4 v234, s[4:5]
	s_waitcnt vmcnt(8)
	s_waitcnt lgkmcnt(0)
	s_barrier
	s_setprio 1
	s_waitcnt lgkmcnt(0)
	v_mfma_f32_16x16x32_bf16 v[128:131], v[140:143], v[172:175], v[128:131]
	v_mfma_f32_16x16x32_bf16 v[120:123], v[148:151], v[172:175], v[120:123]
	v_mfma_f32_16x16x32_bf16 v[112:115], v[140:143], v[180:183], v[112:115]
	v_mfma_f32_16x16x32_bf16 v[104:107], v[148:151], v[180:183], v[104:107]
	v_mfma_f32_16x16x32_bf16 v[96:99], v[140:143], v[188:191], v[96:99]
	v_mfma_f32_16x16x32_bf16 v[88:91], v[148:151], v[188:191], v[88:91]
	v_mfma_f32_16x16x32_bf16 v[80:83], v[140:143], v[202:205], v[80:83]
	v_mfma_f32_16x16x32_bf16 v[72:75], v[148:151], v[202:205], v[72:75]
	v_mfma_f32_16x16x32_bf16 v[128:131], v[144:147], v[176:179], v[128:131]
	v_mfma_f32_16x16x32_bf16 v[120:123], v[152:155], v[176:179], v[120:123]
	v_mfma_f32_16x16x32_bf16 v[112:115], v[144:147], v[184:187], v[112:115]
	v_mfma_f32_16x16x32_bf16 v[104:107], v[152:155], v[184:187], v[104:107]
	v_mfma_f32_16x16x32_bf16 v[96:99], v[144:147], v[192:195], v[96:99]
	v_mfma_f32_16x16x32_bf16 v[88:91], v[152:155], v[192:195], v[88:91]
	v_mfma_f32_16x16x32_bf16 v[80:83], v[144:147], v[222:225], v[80:83]
	v_mfma_f32_16x16x32_bf16 v[72:75], v[152:155], v[222:225], v[72:75]
	s_setprio 0
	s_setprio 1
	v_mfma_f32_16x16x32_bf16 v[64:67], v[156:159], v[172:175], v[64:67]
	v_mfma_f32_16x16x32_bf16 v[60:63], v[164:167], v[172:175], v[60:63]
	v_mfma_f32_16x16x32_bf16 v[56:59], v[156:159], v[180:183], v[56:59]
	v_mfma_f32_16x16x32_bf16 v[52:55], v[164:167], v[180:183], v[52:55]
	v_mfma_f32_16x16x32_bf16 v[44:47], v[156:159], v[188:191], v[44:47]
	v_mfma_f32_16x16x32_bf16 v[40:43], v[164:167], v[188:191], v[40:43]
	v_mfma_f32_16x16x32_bf16 v[36:39], v[156:159], v[202:205], v[36:39]
	v_mfma_f32_16x16x32_bf16 v[32:35], v[164:167], v[202:205], v[32:35]
	v_mfma_f32_16x16x32_bf16 v[64:67], v[160:163], v[176:179], v[64:67]
	v_mfma_f32_16x16x32_bf16 v[60:63], v[168:171], v[176:179], v[60:63]
	v_mfma_f32_16x16x32_bf16 v[56:59], v[160:163], v[184:187], v[56:59]
	v_mfma_f32_16x16x32_bf16 v[52:55], v[168:171], v[184:187], v[52:55]
	v_mfma_f32_16x16x32_bf16 v[44:47], v[160:163], v[192:195], v[44:47]
	v_mfma_f32_16x16x32_bf16 v[40:43], v[168:171], v[192:195], v[40:43]
	v_mfma_f32_16x16x32_bf16 v[36:39], v[160:163], v[222:225], v[36:39]
	v_mfma_f32_16x16x32_bf16 v[32:35], v[168:171], v[222:225], v[32:35]
	s_setprio 0
	s_barrier
	s_add_i32 s4, s64, s9
	v_lshl_add_u64 v[226:227], v[242:243], 0, s[88:89]
	s_mov_b32 m0, s4
	ds_read_b128 v[172:175], v201 offset:49152
	ds_read_b128 v[176:179], v201 offset:50176
	ds_read_b128 v[180:183], v201 offset:51200
	ds_read_b128 v[184:187], v201 offset:52224
	ds_read_b128 v[188:191], v201 offset:53248
	ds_read_b128 v[192:195], v201 offset:54272
	ds_read_b128 v[202:205], v201 offset:55296
	ds_read_b128 v[222:225], v201 offset:56320
	global_load_lds_dwordx4 v[226:227], off
	v_lshl_add_u64 v[226:227], v[244:245], 0, s[88:89]
	s_add_i32 m0, s4, 0x2000
	s_add_i32 s4, s65, s9
	global_load_lds_dwordx4 v[226:227], off
	v_lshl_add_u64 v[226:227], v[246:247], 0, s[88:89]
	s_mov_b32 m0, s4
	s_nop 0
	global_load_lds_dwordx4 v[226:227], off
	v_lshl_add_u64 v[226:227], v[240:241], 0, s[88:89]
	s_add_i32 m0, s4, 0x2000
	s_nop 0
	global_load_lds_dwordx4 v[226:227], off
	v_lshl_add_u64 v[226:227], v[248:249], 0, s[88:89]
	s_mov_b32 m0, s6
	s_nop 0
	global_load_lds_dwordx4 v[226:227], off
	v_lshl_add_u64 v[226:227], v[250:251], 0, s[88:89]
	s_mov_b32 m0, s14
	s_nop 0
	global_load_lds_dwordx4 v[226:227], off
	s_waitcnt vmcnt(8)
	s_waitcnt lgkmcnt(0)
	s_barrier
	s_setprio 1
	s_waitcnt lgkmcnt(0)
	v_mfma_f32_16x16x32_bf16 v[28:31], v[140:143], v[172:175], v[28:31]
	v_mfma_f32_16x16x32_bf16 v[24:27], v[148:151], v[172:175], v[24:27]
	v_mfma_f32_16x16x32_bf16 v[20:23], v[140:143], v[180:183], v[20:23]
	v_mfma_f32_16x16x32_bf16 v[16:19], v[148:151], v[180:183], v[16:19]
	v_mfma_f32_16x16x32_bf16 v[12:15], v[140:143], v[188:191], v[12:15]
	v_mfma_f32_16x16x32_bf16 v[8:11], v[148:151], v[188:191], v[8:11]
	v_mfma_f32_16x16x32_bf16 v[4:7], v[140:143], v[202:205], v[4:7]
	v_mfma_f32_16x16x32_bf16 v[0:3], v[148:151], v[202:205], v[0:3]
	v_mfma_f32_16x16x32_bf16 v[28:31], v[144:147], v[176:179], v[28:31]
	v_mfma_f32_16x16x32_bf16 v[24:27], v[152:155], v[176:179], v[24:27]
	v_mfma_f32_16x16x32_bf16 v[20:23], v[144:147], v[184:187], v[20:23]
	v_mfma_f32_16x16x32_bf16 v[16:19], v[152:155], v[184:187], v[16:19]
	v_mfma_f32_16x16x32_bf16 v[12:15], v[144:147], v[192:195], v[12:15]
	v_mfma_f32_16x16x32_bf16 v[8:11], v[152:155], v[192:195], v[8:11]
	v_mfma_f32_16x16x32_bf16 v[4:7], v[144:147], v[222:225], v[4:7]
	v_mfma_f32_16x16x32_bf16 v[0:3], v[152:155], v[222:225], v[0:3]
	s_setprio 0
	s_setprio 1
	v_mfma_f32_16x16x32_bf16 v[68:71], v[156:159], v[172:175], v[68:71]
	v_mfma_f32_16x16x32_bf16 v[76:79], v[164:167], v[172:175], v[76:79]
	v_mfma_f32_16x16x32_bf16 v[84:87], v[156:159], v[180:183], v[84:87]
	v_mfma_f32_16x16x32_bf16 v[92:95], v[164:167], v[180:183], v[92:95]
	v_mfma_f32_16x16x32_bf16 v[100:103], v[156:159], v[188:191], v[100:103]
	v_mfma_f32_16x16x32_bf16 v[108:111], v[164:167], v[188:191], v[108:111]
	v_mfma_f32_16x16x32_bf16 v[116:119], v[156:159], v[202:205], v[116:119]
	v_mfma_f32_16x16x32_bf16 v[124:127], v[164:167], v[202:205], v[124:127]
	v_mfma_f32_16x16x32_bf16 v[68:71], v[160:163], v[176:179], v[68:71]
	v_mfma_f32_16x16x32_bf16 v[76:79], v[168:171], v[176:179], v[76:79]
	v_mfma_f32_16x16x32_bf16 v[84:87], v[160:163], v[184:187], v[84:87]
	v_mfma_f32_16x16x32_bf16 v[92:95], v[168:171], v[184:187], v[92:95]
	v_mfma_f32_16x16x32_bf16 v[100:103], v[160:163], v[192:195], v[100:103]
	v_mfma_f32_16x16x32_bf16 v[108:111], v[168:171], v[192:195], v[108:111]
	v_mfma_f32_16x16x32_bf16 v[116:119], v[160:163], v[222:225], v[116:119]
	v_mfma_f32_16x16x32_bf16 v[124:127], v[168:171], v[222:225], v[124:127]
	s_setprio 0
	s_barrier
	s_add_u32 s0, s0, 0x100
	s_addc_u32 s1, s1, 0
	s_cmp_ge_u32 s73, s47

.LBB0_447:
	s_andn2_b64 vcc, exec, s[54:55]
	s_cbranch_vccnz .LBB0_449
	s_add_i32 s46, s46, 1
	s_mov_b32 s20, s21
	s_mov_b32 s36, s12
